# v40 + MoE down-GEMM and LN2 phases reuse the expert start-row tables left in LDS by the same layer's MoE gate/up phase (when it ran in the same launch) instead of rebuilding them
# baseline (speedup 1.0000x reference)
.LBB0_1635:
	s_andn2_b64 vcc, exec, s[0:1]
	s_cbranch_vccnz .LBB0_1700
	v_readlane_b32 s0, v253, 61
	s_nop 1
	v_mov_b32_e32 v1, s0
	s_waitcnt vmcnt(0)
	ds_read_b64 v[4:5], v1
	s_waitcnt lgkmcnt(0)
	v_readfirstlane_b32 s4, v5
	v_readfirstlane_b32 s5, v4
	s_and_saveexec_b64 s[0:1], s[90:91]
	s_cbranch_execz .LBB0_1638
	s_mul_i32 s2, s76, 13
	s_add_i32 s2, s2, 10
	s_cmp_le_i32 s72, s2
	s_cbranch_scc1 .LBB0_1638
	s_lshl_b32 s92, s76, 5
	v_readfirstlane_b32 s6, v4
	s_lshl_b64 s[2:3], s[92:93], 2
	v_readfirstlane_b32 s7, v5
	s_add_u32 s6, s6, s2
	s_addc_u32 s7, s7, s3
	s_add_u32 s2, s6, 0x2000
	s_addc_u32 s3, s7, 0
	v_mov_b32_e32 v1, 0x2000
	global_load_dwordx4 v[4:7], v3, s[2:3] offset:48
	global_load_dwordx4 v[8:11], v3, s[2:3] offset:32
	global_load_dwordx4 v[12:15], v3, s[2:3] offset:16
	global_load_dwordx4 v[16:19], v1, s[6:7]
	v_readlane_b32 s6, v254, 31
	v_mov_b32_e32 v20, v3
	v_mov_b32_e32 v24, v3
	s_waitcnt vmcnt(0)
	v_add_u32_e32 v1, 0xff, v17
	v_add_u32_e32 v2, 0xff, v16
	v_lshrrev_b32_e32 v21, 8, v2
	v_lshrrev_b32_e32 v1, 8, v1
	v_and_b32_e32 v25, 0xffffff00, v2
	v_add_u32_e32 v2, 0xff, v18
	v_lshrrev_b32_e32 v2, 8, v2
	v_add_u32_e32 v22, v1, v21
	v_add_u32_e32 v23, v2, v22
	v_mov_b32_e32 v1, s6
	v_readlane_b32 s6, v254, 32
	ds_write_b128 v1, v[20:23]
	v_lshlrev_b32_e32 v26, 8, v22
	v_lshlrev_b32_e32 v27, 8, v23
	v_mov_b32_e32 v1, s6
	ds_write_b128 v1, v[24:27]
	v_add_u32_e32 v1, 0xff, v19
	v_lshrrev_b32_e32 v1, 8, v1
	v_add_u32_e32 v2, 0xff, v12
	v_lshrrev_b32_e32 v2, 8, v2
	v_add_u32_e32 v16, v1, v23
	v_add_u32_e32 v1, 0xff, v13
	v_add_u32_e32 v17, v2, v16
	v_lshrrev_b32_e32 v1, 8, v1
	v_add_u32_e32 v2, 0xff, v14
	v_lshrrev_b32_e32 v2, 8, v2
	v_add_u32_e32 v18, v1, v17
	v_readlane_b32 s6, v254, 33
	v_add_u32_e32 v19, v2, v18
	v_lshlrev_b32_e32 v20, 8, v16
	v_mov_b32_e32 v1, s6
	v_readlane_b32 s6, v254, 34
	v_lshlrev_b32_e32 v21, 8, v17
	ds_write_b128 v1, v[16:19]
	v_lshlrev_b32_e32 v22, 8, v18
	v_lshlrev_b32_e32 v23, 8, v19
	v_mov_b32_e32 v1, s6
	ds_write_b128 v1, v[20:23]
	v_add_u32_e32 v1, 0xff, v15
	v_lshrrev_b32_e32 v1, 8, v1
	v_add_u32_e32 v2, 0xff, v8
	v_lshrrev_b32_e32 v2, 8, v2
	v_add_u32_e32 v12, v1, v19
	v_add_u32_e32 v1, 0xff, v9
	v_add_u32_e32 v13, v2, v12
	v_lshrrev_b32_e32 v1, 8, v1
	v_add_u32_e32 v2, 0xff, v10
	v_lshrrev_b32_e32 v2, 8, v2
	v_add_u32_e32 v14, v1, v13
	v_readlane_b32 s6, v254, 35
	v_add_u32_e32 v15, v2, v14
	v_lshlrev_b32_e32 v16, 8, v12
	v_mov_b32_e32 v1, s6
	v_readlane_b32 s6, v254, 36
	v_lshlrev_b32_e32 v17, 8, v13
	ds_write_b128 v1, v[12:15]
	v_lshlrev_b32_e32 v18, 8, v14
	v_lshlrev_b32_e32 v19, 8, v15
	v_mov_b32_e32 v1, s6
	ds_write_b128 v1, v[16:19]
	v_add_u32_e32 v1, 0xff, v11
	v_lshrrev_b32_e32 v1, 8, v1
	v_add_u32_e32 v2, 0xff, v4
	v_lshrrev_b32_e32 v2, 8, v2
	v_add_u32_e32 v14, v1, v15
	v_add_u32_e32 v1, 0xff, v5
	v_add_u32_e32 v15, v2, v14
	v_lshrrev_b32_e32 v1, 8, v1
	v_add_u32_e32 v2, 0xff, v6
	v_lshrrev_b32_e32 v2, 8, v2
	v_add_u32_e32 v16, v1, v15
	v_readlane_b32 s6, v254, 37
	v_add_u32_e32 v17, v2, v16
	v_lshlrev_b32_e32 v8, 8, v14
	v_mov_b32_e32 v1, s6
	v_readlane_b32 s6, v254, 38
	v_lshlrev_b32_e32 v9, 8, v15
	ds_write_b128 v1, v[14:17]
	v_lshlrev_b32_e32 v10, 8, v16
	v_lshlrev_b32_e32 v11, 8, v17
	v_mov_b32_e32 v1, s6
	ds_write_b128 v1, v[8:11]
	v_add_u32_e32 v1, 0xff, v7
	global_load_dwordx4 v[4:7], v3, s[2:3] offset:112
	global_load_dwordx4 v[8:11], v3, s[2:3] offset:96
	global_load_dwordx4 v[12:15], v3, s[2:3] offset:80
	global_load_dwordx4 v[18:21], v3, s[2:3] offset:64
	v_lshrrev_b32_e32 v1, 8, v1
	v_add_u32_e32 v16, v1, v17
	v_readlane_b32 s2, v254, 39
	v_lshlrev_b32_e32 v22, 8, v16
	s_waitcnt vmcnt(0)
	v_add_u32_e32 v2, 0xff, v18
	v_lshrrev_b32_e32 v2, 8, v2
	v_add_u32_e32 v1, 0xff, v19
	v_add_u32_e32 v17, v2, v16
	v_lshrrev_b32_e32 v1, 8, v1
	v_add_u32_e32 v2, 0xff, v20
	v_lshrrev_b32_e32 v2, 8, v2
	v_add_u32_e32 v18, v1, v17
	v_add_u32_e32 v19, v2, v18
	v_mov_b32_e32 v1, s2
	v_readlane_b32 s2, v254, 40
	v_lshlrev_b32_e32 v23, 8, v17
	ds_write_b128 v1, v[16:19]
	v_lshlrev_b32_e32 v24, 8, v18
	v_lshlrev_b32_e32 v25, 8, v19
	v_mov_b32_e32 v1, s2
	ds_write_b128 v1, v[22:25]
	v_add_u32_e32 v1, 0xff, v21
	v_lshrrev_b32_e32 v1, 8, v1
	v_add_u32_e32 v2, 0xff, v12
	v_lshrrev_b32_e32 v2, 8, v2
	v_add_u32_e32 v16, v1, v19
	v_add_u32_e32 v1, 0xff, v13
	v_add_u32_e32 v17, v2, v16
	v_lshrrev_b32_e32 v1, 8, v1
	v_add_u32_e32 v2, 0xff, v14
	v_lshrrev_b32_e32 v2, 8, v2
	v_add_u32_e32 v18, v1, v17
	v_readlane_b32 s2, v254, 41
	v_add_u32_e32 v19, v2, v18
	v_lshlrev_b32_e32 v20, 8, v16
	v_mov_b32_e32 v1, s2
	v_readlane_b32 s2, v254, 42
	v_lshlrev_b32_e32 v21, 8, v17
	ds_write_b128 v1, v[16:19]
	v_lshlrev_b32_e32 v22, 8, v18
	v_lshlrev_b32_e32 v23, 8, v19
	v_mov_b32_e32 v1, s2
	ds_write_b128 v1, v[20:23]
	v_add_u32_e32 v1, 0xff, v15
	v_lshrrev_b32_e32 v1, 8, v1
	v_add_u32_e32 v2, 0xff, v8
	v_lshrrev_b32_e32 v2, 8, v2
	v_add_u32_e32 v12, v1, v19
	v_add_u32_e32 v1, 0xff, v9
	v_add_u32_e32 v13, v2, v12
	v_lshrrev_b32_e32 v1, 8, v1
	v_add_u32_e32 v2, 0xff, v10
	v_lshrrev_b32_e32 v2, 8, v2
	v_add_u32_e32 v14, v1, v13
	v_readlane_b32 s2, v254, 43
	v_add_u32_e32 v15, v2, v14
	v_lshlrev_b32_e32 v16, 8, v12
	v_mov_b32_e32 v1, s2
	v_readlane_b32 s2, v254, 44
	v_lshlrev_b32_e32 v17, 8, v13
	ds_write_b128 v1, v[12:15]
	v_lshlrev_b32_e32 v18, 8, v14
	v_lshlrev_b32_e32 v19, 8, v15
	v_mov_b32_e32 v1, s2
	ds_write_b128 v1, v[16:19]
	v_add_u32_e32 v1, 0xff, v11
	v_lshrrev_b32_e32 v1, 8, v1
	v_add_u32_e32 v2, 0xff, v4
	v_lshrrev_b32_e32 v2, 8, v2
	v_add_u32_e32 v8, v1, v15
	v_add_u32_e32 v1, 0xff, v5
	v_add_u32_e32 v9, v2, v8
	v_lshrrev_b32_e32 v1, 8, v1
	v_add_u32_e32 v2, 0xff, v6
	v_lshrrev_b32_e32 v2, 8, v2
	v_add_u32_e32 v10, v1, v9
	v_readlane_b32 s2, v254, 45
	v_add_u32_e32 v11, v2, v10
	v_lshlrev_b32_e32 v12, 8, v8
	v_mov_b32_e32 v1, s2
	v_readlane_b32 s2, v254, 46
	v_lshlrev_b32_e32 v13, 8, v9
	ds_write_b128 v1, v[8:11]
	v_lshlrev_b32_e32 v14, 8, v10
	v_lshlrev_b32_e32 v15, 8, v11
	v_mov_b32_e32 v1, s2
	ds_write_b128 v1, v[12:15]
	v_add_u32_e32 v1, 0xff, v7
	v_lshrrev_b32_e32 v1, 8, v1
	v_readlane_b32 s2, v254, 47
	v_add_u32_e32 v1, v1, v11
	s_nop 0
	v_mov_b32_e32 v2, s2
	v_readlane_b32 s2, v254, 48
	ds_write_b32 v2, v1
	v_lshlrev_b32_e32 v1, 8, v1
	v_mov_b32_e32 v2, s2
	ds_write_b32 v2, v1

.LBB0_1701:
	s_and_saveexec_b64 s[0:1], s[90:91]
	s_cbranch_execz .LBB0_1703
	s_mul_i32 s2, s76, 13
	s_add_i32 s2, s2, 10
	s_cmp_le_i32 s72, s2
	s_cbranch_scc1 .LBB0_1703
	v_readlane_b32 s2, v253, 61
	s_lshl_b32 s92, s76, 5
	s_waitcnt vmcnt(0)
	v_mov_b32_e32 v20, v3
	v_mov_b32_e32 v1, s2
	ds_read_b64 v[4:5], v1
	s_lshl_b64 s[2:3], s[92:93], 2
	v_mov_b32_e32 v1, 0x2000
	v_mov_b32_e32 v24, v3
	s_waitcnt lgkmcnt(0)
	v_readfirstlane_b32 s4, v4
	v_readfirstlane_b32 s5, v5
	s_add_u32 s4, s4, s2
	s_addc_u32 s5, s5, s3
	s_add_u32 s2, s4, 0x2000
	s_addc_u32 s3, s5, 0
	global_load_dwordx4 v[4:7], v3, s[2:3] offset:48
	global_load_dwordx4 v[8:11], v3, s[2:3] offset:32
	global_load_dwordx4 v[12:15], v3, s[2:3] offset:16
	global_load_dwordx4 v[16:19], v1, s[4:5]
	v_readlane_b32 s4, v254, 31
	s_waitcnt vmcnt(0)
	v_add_u32_e32 v1, 0xff, v17
	v_add_u32_e32 v2, 0xff, v16
	v_lshrrev_b32_e32 v21, 8, v2
	v_lshrrev_b32_e32 v1, 8, v1
	v_and_b32_e32 v25, 0xffffff00, v2
	v_add_u32_e32 v2, 0xff, v18
	v_lshrrev_b32_e32 v2, 8, v2
	v_add_u32_e32 v22, v1, v21
	v_add_u32_e32 v23, v2, v22
	v_mov_b32_e32 v1, s4
	ds_write_b128 v1, v[20:23]
	v_lshlrev_b32_e32 v26, 8, v22
	v_lshlrev_b32_e32 v27, 8, v23
	v_mov_b32_e32 v1, s28
	ds_write_b128 v1, v[24:27]
	v_add_u32_e32 v1, 0xff, v19
	v_lshrrev_b32_e32 v1, 8, v1
	v_add_u32_e32 v2, 0xff, v12
	v_lshrrev_b32_e32 v2, 8, v2
	v_add_u32_e32 v16, v1, v23
	v_add_u32_e32 v1, 0xff, v13
	v_add_u32_e32 v17, v2, v16
	v_lshrrev_b32_e32 v1, 8, v1
	v_add_u32_e32 v2, 0xff, v14
	v_lshrrev_b32_e32 v2, 8, v2
	v_add_u32_e32 v18, v1, v17
	v_readlane_b32 s4, v254, 33
	v_add_u32_e32 v19, v2, v18
	v_lshlrev_b32_e32 v20, 8, v16
	v_mov_b32_e32 v1, s4
	v_readlane_b32 s4, v254, 34
	v_lshlrev_b32_e32 v21, 8, v17
	ds_write_b128 v1, v[16:19]
	v_lshlrev_b32_e32 v22, 8, v18
	v_lshlrev_b32_e32 v23, 8, v19
	v_mov_b32_e32 v1, s4
	ds_write_b128 v1, v[20:23]
	v_add_u32_e32 v1, 0xff, v15
	v_lshrrev_b32_e32 v1, 8, v1
	v_add_u32_e32 v2, 0xff, v8
	v_lshrrev_b32_e32 v2, 8, v2
	v_add_u32_e32 v12, v1, v19
	v_add_u32_e32 v1, 0xff, v9
	v_add_u32_e32 v13, v2, v12
	v_lshrrev_b32_e32 v1, 8, v1
	v_add_u32_e32 v2, 0xff, v10
	v_lshrrev_b32_e32 v2, 8, v2
	v_add_u32_e32 v14, v1, v13
	v_readlane_b32 s4, v254, 35
	v_add_u32_e32 v15, v2, v14
	v_lshlrev_b32_e32 v16, 8, v12
	v_mov_b32_e32 v1, s4
	v_readlane_b32 s4, v254, 36
	v_lshlrev_b32_e32 v17, 8, v13
	ds_write_b128 v1, v[12:15]
	v_lshlrev_b32_e32 v18, 8, v14
	v_lshlrev_b32_e32 v19, 8, v15
	v_mov_b32_e32 v1, s4
	ds_write_b128 v1, v[16:19]
	v_add_u32_e32 v1, 0xff, v11
	v_lshrrev_b32_e32 v1, 8, v1
	v_add_u32_e32 v2, 0xff, v4
	v_lshrrev_b32_e32 v2, 8, v2
	v_add_u32_e32 v14, v1, v15
	v_add_u32_e32 v1, 0xff, v5
	v_add_u32_e32 v15, v2, v14
	v_lshrrev_b32_e32 v1, 8, v1
	v_add_u32_e32 v2, 0xff, v6
	v_lshrrev_b32_e32 v2, 8, v2
	v_add_u32_e32 v16, v1, v15
	v_readlane_b32 s4, v254, 37
	v_add_u32_e32 v17, v2, v16
	v_lshlrev_b32_e32 v8, 8, v14
	v_mov_b32_e32 v1, s4
	v_readlane_b32 s4, v254, 38
	v_lshlrev_b32_e32 v9, 8, v15
	ds_write_b128 v1, v[14:17]
	v_lshlrev_b32_e32 v10, 8, v16
	v_lshlrev_b32_e32 v11, 8, v17
	v_mov_b32_e32 v1, s4
	ds_write_b128 v1, v[8:11]
	v_add_u32_e32 v1, 0xff, v7
	global_load_dwordx4 v[4:7], v3, s[2:3] offset:112
	global_load_dwordx4 v[8:11], v3, s[2:3] offset:96
	global_load_dwordx4 v[12:15], v3, s[2:3] offset:80
	global_load_dwordx4 v[18:21], v3, s[2:3] offset:64
	v_lshrrev_b32_e32 v1, 8, v1
	v_add_u32_e32 v16, v1, v17
	v_readlane_b32 s2, v254, 39
	v_lshlrev_b32_e32 v22, 8, v16
	s_waitcnt vmcnt(0)
	v_add_u32_e32 v2, 0xff, v18
	v_lshrrev_b32_e32 v2, 8, v2
	v_add_u32_e32 v1, 0xff, v19
	v_add_u32_e32 v17, v2, v16
	v_lshrrev_b32_e32 v1, 8, v1
	v_add_u32_e32 v2, 0xff, v20
	v_lshrrev_b32_e32 v2, 8, v2
	v_add_u32_e32 v18, v1, v17
	v_add_u32_e32 v19, v2, v18
	v_mov_b32_e32 v1, s2
	v_readlane_b32 s2, v254, 40
	v_lshlrev_b32_e32 v23, 8, v17
	ds_write_b128 v1, v[16:19]
	v_lshlrev_b32_e32 v24, 8, v18
	v_lshlrev_b32_e32 v25, 8, v19
	v_mov_b32_e32 v1, s2
	ds_write_b128 v1, v[22:25]
	v_add_u32_e32 v1, 0xff, v21
	v_lshrrev_b32_e32 v1, 8, v1
	v_add_u32_e32 v2, 0xff, v12
	v_lshrrev_b32_e32 v2, 8, v2
	v_add_u32_e32 v16, v1, v19
	v_add_u32_e32 v1, 0xff, v13
	v_add_u32_e32 v17, v2, v16
	v_lshrrev_b32_e32 v1, 8, v1
	v_add_u32_e32 v2, 0xff, v14
	v_lshrrev_b32_e32 v2, 8, v2
	v_add_u32_e32 v18, v1, v17
	v_readlane_b32 s2, v254, 41
	v_add_u32_e32 v19, v2, v18
	v_lshlrev_b32_e32 v20, 8, v16
	v_mov_b32_e32 v1, s2
	v_readlane_b32 s2, v254, 42
	v_lshlrev_b32_e32 v21, 8, v17
	ds_write_b128 v1, v[16:19]
	v_lshlrev_b32_e32 v22, 8, v18
	v_lshlrev_b32_e32 v23, 8, v19
	v_mov_b32_e32 v1, s2
	ds_write_b128 v1, v[20:23]
	v_add_u32_e32 v1, 0xff, v15
	v_lshrrev_b32_e32 v1, 8, v1
	v_add_u32_e32 v2, 0xff, v8
	v_lshrrev_b32_e32 v2, 8, v2
	v_add_u32_e32 v12, v1, v19
	v_add_u32_e32 v1, 0xff, v9
	v_add_u32_e32 v13, v2, v12
	v_lshrrev_b32_e32 v1, 8, v1
	v_add_u32_e32 v2, 0xff, v10
	v_lshrrev_b32_e32 v2, 8, v2
	v_add_u32_e32 v14, v1, v13
	v_readlane_b32 s2, v254, 43
	v_add_u32_e32 v15, v2, v14
	v_lshlrev_b32_e32 v16, 8, v12
	v_mov_b32_e32 v1, s2
	v_readlane_b32 s2, v254, 44
	v_lshlrev_b32_e32 v17, 8, v13
	ds_write_b128 v1, v[12:15]
	v_lshlrev_b32_e32 v18, 8, v14
	v_lshlrev_b32_e32 v19, 8, v15
	v_mov_b32_e32 v1, s2
	ds_write_b128 v1, v[16:19]
	v_add_u32_e32 v1, 0xff, v11
	v_lshrrev_b32_e32 v1, 8, v1
	v_add_u32_e32 v2, 0xff, v4
	v_lshrrev_b32_e32 v2, 8, v2
	v_add_u32_e32 v8, v1, v15
	v_add_u32_e32 v1, 0xff, v5
	v_add_u32_e32 v9, v2, v8
	v_lshrrev_b32_e32 v1, 8, v1
	v_add_u32_e32 v2, 0xff, v6
	v_lshrrev_b32_e32 v2, 8, v2
	v_add_u32_e32 v10, v1, v9
	v_readlane_b32 s2, v254, 45
	v_add_u32_e32 v11, v2, v10
	v_lshlrev_b32_e32 v12, 8, v8
	v_mov_b32_e32 v1, s2
	v_readlane_b32 s2, v254, 46
	v_lshlrev_b32_e32 v13, 8, v9
	ds_write_b128 v1, v[8:11]
	v_lshlrev_b32_e32 v14, 8, v10
	v_lshlrev_b32_e32 v15, 8, v11
	v_mov_b32_e32 v1, s2
	ds_write_b128 v1, v[12:15]
	v_add_u32_e32 v1, 0xff, v7
	v_lshrrev_b32_e32 v1, 8, v1
	v_readlane_b32 s2, v254, 47
	v_add_u32_e32 v1, v1, v11
	s_nop 0
	v_mov_b32_e32 v2, s2
	v_readlane_b32 s2, v254, 48
	ds_write_b32 v2, v1
	v_lshlrev_b32_e32 v1, 8, v1
	v_mov_b32_e32 v2, s2
	ds_write_b32 v2, v1
